# scatter_kernel: quarter-rate v_mul_hi_i32 / v_mul_lo_u32 for /196 and %196 replaced by exact full-rate 24-bit multiplies (indices < 2^17)
# baseline (speedup 1.0000x reference)
.LBB0_9:
	s_or_b64 exec, exec, s[8:9]
	s_mov_b32 s3, 0x5397829d
	s_waitcnt vmcnt(2)
	v_lshlrev_b32_e32 v49, 7, v27
	v_mul_hi_u32_u24_e32 v49, 0xa72f06, v49
	v_lshlrev_b32_e32 v38, 7, v26
	v_mul_hi_u32_u24_e32 v38, 0xa72f06, v38
	v_lshrrev_b32_e32 v50, 31, v49
	v_ashrrev_i32_e32 v49, 6, v49
	v_lshrrev_b32_e32 v39, 31, v38
	v_ashrrev_i32_e32 v38, 6, v38
	v_add_u32_e32 v56, v49, v50
	v_lshlrev_b32_e32 v49, 7, v28
	v_mul_hi_u32_u24_e32 v49, 0xa72f06, v49
	v_add_u32_e32 v63, v38, v39
	v_mov_b32_e32 v38, 0x17700
	v_lshrrev_b32_e32 v50, 31, v49
	v_ashrrev_i32_e32 v49, 6, v49
	v_lshl_add_u32 v61, v63, 2, v38
	v_mov_b32_e32 v39, 1
	v_add_u32_e32 v57, v49, v50
	v_lshlrev_b32_e32 v49, 7, v29
	v_mul_hi_u32_u24_e32 v49, 0xa72f06, v49
	ds_add_rtn_u32 v62, v61, v39
	v_lshl_add_u32 v60, v56, 2, v38
	v_lshrrev_b32_e32 v50, 31, v49
	v_ashrrev_i32_e32 v49, 6, v49
	ds_add_rtn_u32 v53, v60, v39
	v_lshl_add_u32 v59, v57, 2, v38
	v_add_u32_e32 v55, v49, v50
	ds_add_rtn_u32 v54, v59, v39
	v_lshl_add_u32 v58, v55, 2, v38
	ds_add_rtn_u32 v52, v58, v39
	v_mov_b32_e32 v49, 0
	v_mov_b32_e32 v50, 0
	v_mov_b32_e32 v51, 0
	s_and_saveexec_b64 s[8:9], s[6:7]
	s_cbranch_execz .LBB0_11
	v_lshlrev_b32_e32 v48, 7, v18
	v_mul_hi_u32_u24_e32 v48, 0xa72f06, v48
	v_lshrrev_b32_e32 v49, 31, v48
	v_ashrrev_i32_e32 v48, 6, v48
	v_add_u32_e32 v48, v48, v49
	v_lshlrev_b32_e32 v49, 7, v19
	v_mul_hi_u32_u24_e32 v49, 0xa72f06, v49
	v_lshrrev_b32_e32 v50, 31, v49
	v_ashrrev_i32_e32 v49, 6, v49
	v_add_u32_e32 v49, v49, v50
	v_lshlrev_b32_e32 v50, 7, v20
	v_mul_hi_u32_u24_e32 v50, 0xa72f06, v50
	v_lshrrev_b32_e32 v51, 31, v50
	v_ashrrev_i32_e32 v50, 6, v50
	v_lshl_add_u32 v48, v48, 2, v38
	v_add_u32_e32 v50, v50, v51
	v_lshlrev_b32_e32 v51, 7, v21
	v_mul_hi_u32_u24_e32 v51, 0xa72f06, v51
	ds_add_rtn_u32 v48, v48, v39
	v_lshl_add_u32 v49, v49, 2, v38
	v_lshrrev_b32_e32 v64, 31, v51
	v_ashrrev_i32_e32 v51, 6, v51
	ds_add_rtn_u32 v49, v49, v39
	v_lshl_add_u32 v50, v50, 2, v38
	v_add_u32_e32 v51, v51, v64
	ds_add_rtn_u32 v50, v50, v39
	v_lshl_add_u32 v38, v51, 2, v38
	ds_add_rtn_u32 v51, v38, v39

.LBB0_21:
	s_or_b64 exec, exec, s[10:11]
	s_movk_i32 s3, 0xc4
	v_mul_u32_u24_e32 v38, 0xc4, v63
	v_sub_u32_e32 v26, v26, v38
	s_waitcnt lgkmcnt(0)
	s_barrier
	s_waitcnt vmcnt(1)
	v_lshl_or_b32 v38, v26, 19, v30
	ds_read_b32 v26, v61
	v_lshlrev_b32_e32 v30, 3, v62
	s_waitcnt vmcnt(0)
	v_mov_b32_e32 v39, v34
	ds_read_b32 v60, v60
	ds_read_b32 v59, v59
	ds_read_b32 v58, v58
	s_waitcnt lgkmcnt(3)
	v_lshl_add_u32 v26, v26, 3, v30
	ds_write_b64 v26, v[38:39] offset:32000
	v_mul_u32_u24_e32 v26, 0xc4, v56
	v_sub_u32_e32 v26, v27, v26
	v_lshl_or_b32 v34, v26, 19, v31
	v_lshlrev_b32_e32 v26, 3, v53
	s_waitcnt lgkmcnt(3)
	v_lshl_add_u32 v26, v60, 3, v26
	ds_write_b64 v26, v[34:35] offset:32000
	v_mul_u32_u24_e32 v26, 0xc4, v57
	v_sub_u32_e32 v26, v28, v26
	v_lshlrev_b32_e32 v27, 3, v54
	v_lshl_or_b32 v26, v26, 19, v32
	s_waitcnt lgkmcnt(3)
	v_lshl_add_u32 v28, v59, 3, v27
	v_mov_b32_e32 v27, v36
	ds_write_b64 v28, v[26:27] offset:32000
	v_mul_u32_u24_e32 v26, 0xc4, v55
	v_sub_u32_e32 v26, v29, v26
	v_lshl_or_b32 v36, v26, 19, v33
	v_lshlrev_b32_e32 v26, 3, v52
	s_waitcnt lgkmcnt(3)
	v_lshl_add_u32 v26, v58, 3, v26
	ds_write_b64 v26, v[36:37] offset:32000
	s_and_saveexec_b64 s[4:5], s[6:7]
	s_cbranch_execz .LBB0_23
	s_mov_b32 s6, 0x5397829d
	v_lshlrev_b32_e32 v26, 7, v18
	v_mul_hi_u32_u24_e32 v26, 0xa72f06, v26
	v_lshrrev_b32_e32 v27, 31, v26
	v_ashrrev_i32_e32 v26, 6, v26
	v_add_u32_e32 v27, v26, v27
	v_mul_u32_u24_e32 v26, 0xc4, v27
	v_sub_u32_e32 v18, v18, v26
	v_lshl_or_b32 v26, v18, 19, v22
	v_mov_b32_e32 v18, 0x17700
	v_lshl_add_u32 v22, v27, 2, v18
	ds_read_b32 v22, v22
	v_lshlrev_b32_e32 v28, 7, v19
	v_mul_hi_u32_u24_e32 v28, 0xa72f06, v28
	v_lshlrev_b32_e32 v30, 7, v20
	v_mul_hi_u32_u24_e32 v30, 0xa72f06, v30
	v_lshlrev_b32_e32 v32, 7, v21
	v_mul_hi_u32_u24_e32 v32, 0xa72f06, v32
	v_lshrrev_b32_e32 v29, 31, v28
	v_ashrrev_i32_e32 v28, 6, v28
	v_lshrrev_b32_e32 v31, 31, v30
	v_ashrrev_i32_e32 v30, 6, v30
	v_lshrrev_b32_e32 v33, 31, v32
	v_ashrrev_i32_e32 v32, 6, v32
	v_add_u32_e32 v28, v28, v29
	v_add_u32_e32 v30, v30, v31
	v_add_u32_e32 v32, v32, v33
	v_lshl_add_u32 v29, v28, 2, v18
	v_lshl_add_u32 v31, v30, 2, v18
	v_lshl_add_u32 v18, v32, 2, v18
	v_lshlrev_b32_e32 v27, 3, v48
	ds_read_b32 v29, v29
	ds_read_b32 v31, v31
	ds_read_b32 v18, v18
	s_waitcnt lgkmcnt(3)
	v_lshl_add_u32 v22, v22, 3, v27
	v_mov_b32_e32 v27, v14
	v_mul_u32_u24_e32 v14, 0xc4, v28
	v_sub_u32_e32 v14, v19, v14
	v_lshlrev_b32_e32 v19, 3, v49
	v_lshl_or_b32 v14, v14, 19, v23
	s_waitcnt lgkmcnt(2)
	v_lshl_add_u32 v19, v29, 3, v19
	ds_write_b64 v22, v[26:27] offset:32000
	ds_write_b64 v19, v[14:15] offset:32000
	v_mul_u32_u24_e32 v14, 0xc4, v30
	v_sub_u32_e32 v14, v20, v14
	v_lshlrev_b32_e32 v15, 3, v50
	v_lshl_or_b32 v14, v14, 19, v24
	s_waitcnt lgkmcnt(3)
	v_lshl_add_u32 v19, v31, 3, v15
	v_mov_b32_e32 v15, v16
	ds_write_b64 v19, v[14:15] offset:32000
	v_mul_u32_u24_e32 v14, 0xc4, v32
	v_sub_u32_e32 v14, v21, v14
	v_lshl_or_b32 v16, v14, 19, v25
	v_lshlrev_b32_e32 v14, 3, v51
	s_waitcnt lgkmcnt(3)
	v_lshl_add_u32 v14, v18, 3, v14
	ds_write_b64 v14, v[16:17] offset:32000
